# router top-8 rank: 15 branchy EXEC-masked 4-candidate blocks replaced by compare/select counting (on top of v73)
# speedup vs baseline: 1.0031x; 1.0031x over previous
.LBB0_1053:
	ds_read_b128 v[2:5], v115
	s_waitcnt lgkmcnt(0)
	v_cmp_eq_f32_e64 s[26:27], v2, v8
	v_cmp_gt_f32_e64 s[28:29], v2, v8
	s_nop 0
	v_cndmask_b32_e64 v10, 0, v153, s[26:27]
	v_cndmask_b32_e64 v10, v10, 1, s[28:29]
	v_add_u32_e32 v9, v9, v10
	v_cmp_eq_f32_e64 s[26:27], v3, v8
	v_cmp_gt_f32_e64 s[28:29], v3, v8
	s_nop 0
	v_cndmask_b32_e64 v10, 0, v154, s[26:27]
	v_cndmask_b32_e64 v10, v10, 1, s[28:29]
	v_add_u32_e32 v9, v9, v10
	v_cmp_eq_f32_e64 s[26:27], v4, v8
	v_cmp_gt_f32_e64 s[28:29], v4, v8
	s_nop 0
	v_cndmask_b32_e64 v10, 0, v155, s[26:27]
	v_cndmask_b32_e64 v10, v10, 1, s[28:29]
	v_add_u32_e32 v9, v9, v10
	v_cmp_eq_f32_e64 s[26:27], v5, v8
	v_cmp_gt_f32_e64 s[28:29], v5, v8
	s_nop 0
	v_cndmask_b32_e64 v10, 0, v156, s[26:27]
	v_cndmask_b32_e64 v10, v10, 1, s[28:29]
	v_add_u32_e32 v9, v9, v10
	s_and_b32 s40, vcc_lo, 16
	s_cmp_eq_u64 s[40:41], 0
	s_cbranch_scc1 .LBB0_1035
.LBB0_1070:
	ds_read_b128 v[2:5], v115 offset:16
	s_waitcnt lgkmcnt(0)
	v_cmp_eq_f32_e64 s[26:27], v2, v8
	v_cmp_gt_f32_e64 s[28:29], v2, v8
	s_nop 0
	v_cndmask_b32_e64 v10, 0, v157, s[26:27]
	v_cndmask_b32_e64 v10, v10, 1, s[28:29]
	v_add_u32_e32 v9, v9, v10
	v_cmp_eq_f32_e64 s[26:27], v3, v8
	v_cmp_gt_f32_e64 s[28:29], v3, v8
	s_nop 0
	v_cndmask_b32_e64 v10, 0, v158, s[26:27]
	v_cndmask_b32_e64 v10, v10, 1, s[28:29]
	v_add_u32_e32 v9, v9, v10
	v_cmp_eq_f32_e64 s[26:27], v4, v8
	v_cmp_gt_f32_e64 s[28:29], v4, v8
	s_nop 0
	v_cndmask_b32_e64 v10, 0, v159, s[26:27]
	v_cndmask_b32_e64 v10, v10, 1, s[28:29]
	v_add_u32_e32 v9, v9, v10
	v_cmp_eq_f32_e64 s[26:27], v5, v8
	v_cmp_gt_f32_e64 s[28:29], v5, v8
	s_nop 0
	v_cndmask_b32_e64 v10, 0, v160, s[26:27]
	v_cndmask_b32_e64 v10, v10, 1, s[28:29]
	v_add_u32_e32 v9, v9, v10
	s_and_b32 s40, vcc_lo, 0x100
	s_cmp_eq_u64 s[40:41], 0
	s_cbranch_scc1 .LBB0_1036
.LBB0_1087:
	ds_read_b128 v[2:5], v115 offset:32
	s_waitcnt lgkmcnt(0)
	v_cmp_eq_f32_e64 s[26:27], v2, v8
	v_cmp_gt_f32_e64 s[28:29], v2, v8
	s_nop 0
	v_cndmask_b32_e64 v10, 0, v161, s[26:27]
	v_cndmask_b32_e64 v10, v10, 1, s[28:29]
	v_add_u32_e32 v9, v9, v10
	v_cmp_eq_f32_e64 s[26:27], v3, v8
	v_cmp_gt_f32_e64 s[28:29], v3, v8
	s_nop 0
	v_cndmask_b32_e64 v10, 0, v162, s[26:27]
	v_cndmask_b32_e64 v10, v10, 1, s[28:29]
	v_add_u32_e32 v9, v9, v10
	v_cmp_eq_f32_e64 s[26:27], v4, v8
	v_cmp_gt_f32_e64 s[28:29], v4, v8
	s_nop 0
	v_cndmask_b32_e64 v10, 0, v163, s[26:27]
	v_cndmask_b32_e64 v10, v10, 1, s[28:29]
	v_add_u32_e32 v9, v9, v10
	v_cmp_eq_f32_e64 s[26:27], v5, v8
	v_cmp_gt_f32_e64 s[28:29], v5, v8
	s_nop 0
	v_cndmask_b32_e64 v10, 0, v164, s[26:27]
	v_cndmask_b32_e64 v10, v10, 1, s[28:29]
	v_add_u32_e32 v9, v9, v10
	s_and_b32 s40, vcc_lo, 0x1000
	s_cmp_eq_u64 s[40:41], 0
	s_cbranch_scc1 .LBB0_1037
.LBB0_1104:
	ds_read_b128 v[2:5], v115 offset:48
	s_waitcnt lgkmcnt(0)
	v_cmp_eq_f32_e64 s[26:27], v2, v8
	v_cmp_gt_f32_e64 s[28:29], v2, v8
	s_nop 0
	v_cndmask_b32_e64 v10, 0, v165, s[26:27]
	v_cndmask_b32_e64 v10, v10, 1, s[28:29]
	v_add_u32_e32 v9, v9, v10
	v_cmp_eq_f32_e64 s[26:27], v3, v8
	v_cmp_gt_f32_e64 s[28:29], v3, v8
	s_nop 0
	v_cndmask_b32_e64 v10, 0, v166, s[26:27]
	v_cndmask_b32_e64 v10, v10, 1, s[28:29]
	v_add_u32_e32 v9, v9, v10
	v_cmp_eq_f32_e64 s[26:27], v4, v8
	v_cmp_gt_f32_e64 s[28:29], v4, v8
	s_nop 0
	v_cndmask_b32_e64 v10, 0, v167, s[26:27]
	v_cndmask_b32_e64 v10, v10, 1, s[28:29]
	v_add_u32_e32 v9, v9, v10
	v_cmp_eq_f32_e64 s[26:27], v5, v8
	v_cmp_gt_f32_e64 s[28:29], v5, v8
	s_nop 0
	v_cndmask_b32_e64 v10, 0, v168, s[26:27]
	v_cndmask_b32_e64 v10, v10, 1, s[28:29]
	v_add_u32_e32 v9, v9, v10
	s_and_b32 s40, vcc_lo, 0x10000
	s_cmp_eq_u64 s[40:41], 0
	s_cbranch_scc1 .LBB0_1038
.LBB0_1121:
	ds_read_b128 v[2:5], v115 offset:64
	s_waitcnt lgkmcnt(0)
	v_cmp_eq_f32_e64 s[26:27], v2, v8
	v_cmp_gt_f32_e64 s[28:29], v2, v8
	s_nop 0
	v_cndmask_b32_e64 v10, 0, v169, s[26:27]
	v_cndmask_b32_e64 v10, v10, 1, s[28:29]
	v_add_u32_e32 v9, v9, v10
	v_cmp_eq_f32_e64 s[26:27], v3, v8
	v_cmp_gt_f32_e64 s[28:29], v3, v8
	s_nop 0
	v_cndmask_b32_e64 v10, 0, v170, s[26:27]
	v_cndmask_b32_e64 v10, v10, 1, s[28:29]
	v_add_u32_e32 v9, v9, v10
	v_cmp_eq_f32_e64 s[26:27], v4, v8
	v_cmp_gt_f32_e64 s[28:29], v4, v8
	s_nop 0
	v_cndmask_b32_e64 v10, 0, v171, s[26:27]
	v_cndmask_b32_e64 v10, v10, 1, s[28:29]
	v_add_u32_e32 v9, v9, v10
	v_cmp_eq_f32_e64 s[26:27], v5, v8
	v_cmp_gt_f32_e64 s[28:29], v5, v8
	s_nop 0
	v_cndmask_b32_e64 v10, 0, v172, s[26:27]
	v_cndmask_b32_e64 v10, v10, 1, s[28:29]
	v_add_u32_e32 v9, v9, v10
	s_and_b32 s40, vcc_lo, 0x100000
	s_cmp_eq_u64 s[40:41], 0
	s_cbranch_scc1 .LBB0_1039
.LBB0_1138:
	ds_read_b128 v[2:5], v115 offset:80
	s_waitcnt lgkmcnt(0)
	v_cmp_eq_f32_e64 s[26:27], v2, v8
	v_cmp_gt_f32_e64 s[28:29], v2, v8
	s_nop 0
	v_cndmask_b32_e64 v10, 0, v173, s[26:27]
	v_cndmask_b32_e64 v10, v10, 1, s[28:29]
	v_add_u32_e32 v9, v9, v10
	v_cmp_eq_f32_e64 s[26:27], v3, v8
	v_cmp_gt_f32_e64 s[28:29], v3, v8
	s_nop 0
	v_cndmask_b32_e64 v10, 0, v174, s[26:27]
	v_cndmask_b32_e64 v10, v10, 1, s[28:29]
	v_add_u32_e32 v9, v9, v10
	v_cmp_eq_f32_e64 s[26:27], v4, v8
	v_cmp_gt_f32_e64 s[28:29], v4, v8
	s_nop 0
	v_cndmask_b32_e64 v10, 0, v175, s[26:27]
	v_cndmask_b32_e64 v10, v10, 1, s[28:29]
	v_add_u32_e32 v9, v9, v10
	v_cmp_eq_f32_e64 s[26:27], v5, v8
	v_cmp_gt_f32_e64 s[28:29], v5, v8
	s_nop 0
	v_cndmask_b32_e64 v10, 0, v176, s[26:27]
	v_cndmask_b32_e64 v10, v10, 1, s[28:29]
	v_add_u32_e32 v9, v9, v10
	s_and_b32 s40, vcc_lo, 0x1000000
	s_cmp_eq_u64 s[40:41], 0
	s_cbranch_scc1 .LBB0_1040
.LBB0_1155:
	ds_read_b128 v[2:5], v115 offset:96
	s_waitcnt lgkmcnt(0)
	v_cmp_eq_f32_e64 s[26:27], v2, v8
	v_cmp_gt_f32_e64 s[28:29], v2, v8
	s_nop 0
	v_cndmask_b32_e64 v10, 0, v177, s[26:27]
	v_cndmask_b32_e64 v10, v10, 1, s[28:29]
	v_add_u32_e32 v9, v9, v10
	v_cmp_eq_f32_e64 s[26:27], v3, v8
	v_cmp_gt_f32_e64 s[28:29], v3, v8
	s_nop 0
	v_cndmask_b32_e64 v10, 0, v178, s[26:27]
	v_cndmask_b32_e64 v10, v10, 1, s[28:29]
	v_add_u32_e32 v9, v9, v10
	v_cmp_eq_f32_e64 s[26:27], v4, v8
	v_cmp_gt_f32_e64 s[28:29], v4, v8
	s_nop 0
	v_cndmask_b32_e64 v10, 0, v179, s[26:27]
	v_cndmask_b32_e64 v10, v10, 1, s[28:29]
	v_add_u32_e32 v9, v9, v10
	v_cmp_eq_f32_e64 s[26:27], v5, v8
	v_cmp_gt_f32_e64 s[28:29], v5, v8
	s_nop 0
	v_cndmask_b32_e64 v10, 0, v180, s[26:27]
	v_cndmask_b32_e64 v10, v10, 1, s[28:29]
	v_add_u32_e32 v9, v9, v10
	s_and_b32 s40, vcc_lo, 0x10000000
	s_cmp_eq_u64 s[40:41], 0
	s_cbranch_scc1 .LBB0_1041
.LBB0_1172:
	ds_read_b128 v[2:5], v115 offset:112
	s_waitcnt lgkmcnt(0)
	v_cmp_eq_f32_e64 s[26:27], v2, v8
	v_cmp_gt_f32_e64 s[28:29], v2, v8
	s_nop 0
	v_cndmask_b32_e64 v10, 0, v181, s[26:27]
	v_cndmask_b32_e64 v10, v10, 1, s[28:29]
	v_add_u32_e32 v9, v9, v10
	v_cmp_eq_f32_e64 s[26:27], v3, v8
	v_cmp_gt_f32_e64 s[28:29], v3, v8
	s_nop 0
	v_cndmask_b32_e64 v10, 0, v182, s[26:27]
	v_cndmask_b32_e64 v10, v10, 1, s[28:29]
	v_add_u32_e32 v9, v9, v10
	v_cmp_eq_f32_e64 s[26:27], v4, v8
	v_cmp_gt_f32_e64 s[28:29], v4, v8
	s_nop 0
	v_cndmask_b32_e64 v10, 0, v183, s[26:27]
	v_cndmask_b32_e64 v10, v10, 1, s[28:29]
	v_add_u32_e32 v9, v9, v10
	v_cmp_eq_f32_e64 s[26:27], v5, v8
	v_cmp_gt_f32_e64 s[28:29], v5, v8
	s_nop 0
	v_cndmask_b32_e64 v10, 0, v184, s[26:27]
	v_cndmask_b32_e64 v10, v10, 1, s[28:29]
	v_add_u32_e32 v9, v9, v10
	s_and_b32 s27, vcc_hi, 1
	s_mov_b32 s26, s41
	s_cmp_eq_u64 s[26:27], 0
	s_cbranch_scc1 .LBB0_1042
.LBB0_1189:
	ds_read_b128 v[2:5], v115 offset:128
	s_waitcnt lgkmcnt(0)
	v_cmp_eq_f32_e64 s[26:27], v2, v8
	v_cmp_gt_f32_e64 s[28:29], v2, v8
	s_nop 0
	v_cndmask_b32_e64 v10, 0, v185, s[26:27]
	v_cndmask_b32_e64 v10, v10, 1, s[28:29]
	v_add_u32_e32 v9, v9, v10
	v_cmp_eq_f32_e64 s[26:27], v3, v8
	v_cmp_gt_f32_e64 s[28:29], v3, v8
	s_nop 0
	v_cndmask_b32_e64 v10, 0, v186, s[26:27]
	v_cndmask_b32_e64 v10, v10, 1, s[28:29]
	v_add_u32_e32 v9, v9, v10
	v_cmp_eq_f32_e64 s[26:27], v4, v8
	v_cmp_gt_f32_e64 s[28:29], v4, v8
	s_nop 0
	v_cndmask_b32_e64 v10, 0, v187, s[26:27]
	v_cndmask_b32_e64 v10, v10, 1, s[28:29]
	v_add_u32_e32 v9, v9, v10
	v_cmp_eq_f32_e64 s[26:27], v5, v8
	v_cmp_gt_f32_e64 s[28:29], v5, v8
	s_nop 0
	v_cndmask_b32_e64 v10, 0, v188, s[26:27]
	v_cndmask_b32_e64 v10, v10, 1, s[28:29]
	v_add_u32_e32 v9, v9, v10
	s_and_b32 s27, vcc_hi, 16
	s_mov_b32 s26, s41
	s_cmp_eq_u64 s[26:27], 0
	s_cbranch_scc1 .LBB0_1043
.LBB0_1206:
	ds_read_b128 v[2:5], v115 offset:144
	s_waitcnt lgkmcnt(0)
	v_cmp_eq_f32_e64 s[26:27], v2, v8
	v_cmp_gt_f32_e64 s[28:29], v2, v8
	s_nop 0
	v_cndmask_b32_e64 v10, 0, v189, s[26:27]
	v_cndmask_b32_e64 v10, v10, 1, s[28:29]
	v_add_u32_e32 v9, v9, v10
	v_cmp_eq_f32_e64 s[26:27], v3, v8
	v_cmp_gt_f32_e64 s[28:29], v3, v8
	s_nop 0
	v_cndmask_b32_e64 v10, 0, v190, s[26:27]
	v_cndmask_b32_e64 v10, v10, 1, s[28:29]
	v_add_u32_e32 v9, v9, v10
	v_cmp_eq_f32_e64 s[26:27], v4, v8
	v_cmp_gt_f32_e64 s[28:29], v4, v8
	s_nop 0
	v_cndmask_b32_e64 v10, 0, v191, s[26:27]
	v_cndmask_b32_e64 v10, v10, 1, s[28:29]
	v_add_u32_e32 v9, v9, v10
	v_cmp_eq_f32_e64 s[26:27], v5, v8
	v_cmp_gt_f32_e64 s[28:29], v5, v8
	s_nop 0
	v_cndmask_b32_e64 v10, 0, v192, s[26:27]
	v_cndmask_b32_e64 v10, v10, 1, s[28:29]
	v_add_u32_e32 v9, v9, v10
	s_and_b32 s27, vcc_hi, 0x100
	s_mov_b32 s26, s41
	s_cmp_eq_u64 s[26:27], 0
	s_cbranch_scc1 .LBB0_1044
.LBB0_1223:
	ds_read_b128 v[2:5], v115 offset:160
	s_waitcnt lgkmcnt(0)
	v_cmp_eq_f32_e64 s[26:27], v2, v8
	v_cmp_gt_f32_e64 s[28:29], v2, v8
	s_nop 0
	v_cndmask_b32_e64 v10, 0, v193, s[26:27]
	v_cndmask_b32_e64 v10, v10, 1, s[28:29]
	v_add_u32_e32 v9, v9, v10
	v_cmp_eq_f32_e64 s[26:27], v3, v8
	v_cmp_gt_f32_e64 s[28:29], v3, v8
	s_nop 0
	v_cndmask_b32_e64 v10, 0, v194, s[26:27]
	v_cndmask_b32_e64 v10, v10, 1, s[28:29]
	v_add_u32_e32 v9, v9, v10
	v_cmp_eq_f32_e64 s[26:27], v4, v8
	v_cmp_gt_f32_e64 s[28:29], v4, v8
	s_nop 0
	v_cndmask_b32_e64 v10, 0, v195, s[26:27]
	v_cndmask_b32_e64 v10, v10, 1, s[28:29]
	v_add_u32_e32 v9, v9, v10
	v_cmp_eq_f32_e64 s[26:27], v5, v8
	v_cmp_gt_f32_e64 s[28:29], v5, v8
	s_nop 0
	v_cndmask_b32_e64 v10, 0, v196, s[26:27]
	v_cndmask_b32_e64 v10, v10, 1, s[28:29]
	v_add_u32_e32 v9, v9, v10
	s_and_b32 s27, vcc_hi, 0x1000
	s_mov_b32 s26, s41
	s_cmp_eq_u64 s[26:27], 0
	s_cbranch_scc1 .LBB0_1045
.LBB0_1240:
	ds_read_b128 v[2:5], v115 offset:176
	s_waitcnt lgkmcnt(0)
	v_cmp_eq_f32_e64 s[26:27], v2, v8
	v_cmp_gt_f32_e64 s[28:29], v2, v8
	s_nop 0
	v_cndmask_b32_e64 v10, 0, v197, s[26:27]
	v_cndmask_b32_e64 v10, v10, 1, s[28:29]
	v_add_u32_e32 v9, v9, v10
	v_cmp_eq_f32_e64 s[26:27], v3, v8
	v_cmp_gt_f32_e64 s[28:29], v3, v8
	s_nop 0
	v_cndmask_b32_e64 v10, 0, v198, s[26:27]
	v_cndmask_b32_e64 v10, v10, 1, s[28:29]
	v_add_u32_e32 v9, v9, v10
	v_cmp_eq_f32_e64 s[26:27], v4, v8
	v_cmp_gt_f32_e64 s[28:29], v4, v8
	s_nop 0
	v_cndmask_b32_e64 v10, 0, v199, s[26:27]
	v_cndmask_b32_e64 v10, v10, 1, s[28:29]
	v_add_u32_e32 v9, v9, v10
	v_cmp_eq_f32_e64 s[26:27], v5, v8
	v_cmp_gt_f32_e64 s[28:29], v5, v8
	s_nop 0
	v_cndmask_b32_e64 v10, 0, v200, s[26:27]
	v_cndmask_b32_e64 v10, v10, 1, s[28:29]
	v_add_u32_e32 v9, v9, v10
	s_and_b32 s27, vcc_hi, 0x10000
	s_mov_b32 s26, s41
	s_cmp_eq_u64 s[26:27], 0
	s_cbranch_scc1 .LBB0_1046
.LBB0_1257:
	ds_read_b128 v[2:5], v115 offset:192
	s_waitcnt lgkmcnt(0)
	v_cmp_eq_f32_e64 s[26:27], v2, v8
	v_cmp_gt_f32_e64 s[28:29], v2, v8
	s_nop 0
	v_cndmask_b32_e64 v10, 0, v201, s[26:27]
	v_cndmask_b32_e64 v10, v10, 1, s[28:29]
	v_add_u32_e32 v9, v9, v10
	v_cmp_eq_f32_e64 s[26:27], v3, v8
	v_cmp_gt_f32_e64 s[28:29], v3, v8
	s_nop 0
	v_cndmask_b32_e64 v10, 0, v202, s[26:27]
	v_cndmask_b32_e64 v10, v10, 1, s[28:29]
	v_add_u32_e32 v9, v9, v10
	v_cmp_eq_f32_e64 s[26:27], v4, v8
	v_cmp_gt_f32_e64 s[28:29], v4, v8
	s_nop 0
	v_cndmask_b32_e64 v10, 0, v203, s[26:27]
	v_cndmask_b32_e64 v10, v10, 1, s[28:29]
	v_add_u32_e32 v9, v9, v10
	v_cmp_eq_f32_e64 s[26:27], v5, v8
	v_cmp_gt_f32_e64 s[28:29], v5, v8
	s_nop 0
	v_cndmask_b32_e64 v10, 0, v204, s[26:27]
	v_cndmask_b32_e64 v10, v10, 1, s[28:29]
	v_add_u32_e32 v9, v9, v10
	s_and_b32 s27, vcc_hi, 0x100000
	s_mov_b32 s26, s41
	s_cmp_eq_u64 s[26:27], 0
	s_cbranch_scc1 .LBB0_1047
.LBB0_1274:
	ds_read_b128 v[2:5], v115 offset:208
	s_waitcnt lgkmcnt(0)
	v_cmp_eq_f32_e64 s[26:27], v2, v8
	v_cmp_gt_f32_e64 s[28:29], v2, v8
	s_nop 0
	v_cndmask_b32_e64 v10, 0, v205, s[26:27]
	v_cndmask_b32_e64 v10, v10, 1, s[28:29]
	v_add_u32_e32 v9, v9, v10
	v_cmp_eq_f32_e64 s[26:27], v3, v8
	v_cmp_gt_f32_e64 s[28:29], v3, v8
	s_nop 0
	v_cndmask_b32_e64 v10, 0, v206, s[26:27]
	v_cndmask_b32_e64 v10, v10, 1, s[28:29]
	v_add_u32_e32 v9, v9, v10
	v_cmp_eq_f32_e64 s[26:27], v4, v8
	v_cmp_gt_f32_e64 s[28:29], v4, v8
	s_nop 0
	v_cndmask_b32_e64 v10, 0, v207, s[26:27]
	v_cndmask_b32_e64 v10, v10, 1, s[28:29]
	v_add_u32_e32 v9, v9, v10
	v_cmp_eq_f32_e64 s[26:27], v5, v8
	v_cmp_gt_f32_e64 s[28:29], v5, v8
	s_nop 0
	v_cndmask_b32_e64 v10, 0, v208, s[26:27]
	v_cndmask_b32_e64 v10, v10, 1, s[28:29]
	v_add_u32_e32 v9, v9, v10
	s_and_b32 s27, vcc_hi, 0x1000000
	s_mov_b32 s26, s41
	s_cmp_eq_u64 s[26:27], 0
	s_cbranch_scc1 .LBB0_1048
.LBB0_1291:
	ds_read_b128 v[2:5], v115 offset:224
	s_waitcnt lgkmcnt(0)
	v_cmp_eq_f32_e64 s[26:27], v2, v8
	v_cmp_gt_f32_e64 s[28:29], v2, v8
	s_nop 0
	v_cndmask_b32_e64 v10, 0, v209, s[26:27]
	v_cndmask_b32_e64 v10, v10, 1, s[28:29]
	v_add_u32_e32 v9, v9, v10
	v_cmp_eq_f32_e64 s[26:27], v3, v8
	v_cmp_gt_f32_e64 s[28:29], v3, v8
	s_nop 0
	v_cndmask_b32_e64 v10, 0, v210, s[26:27]
	v_cndmask_b32_e64 v10, v10, 1, s[28:29]
	v_add_u32_e32 v9, v9, v10
	v_cmp_eq_f32_e64 s[26:27], v4, v8
	v_cmp_gt_f32_e64 s[28:29], v4, v8
	s_nop 0
	v_cndmask_b32_e64 v10, 0, v211, s[26:27]
	v_cndmask_b32_e64 v10, v10, 1, s[28:29]
	v_add_u32_e32 v9, v9, v10
	v_cmp_eq_f32_e64 s[26:27], v5, v8
	v_cmp_gt_f32_e64 s[28:29], v5, v8
	s_nop 0
	v_cndmask_b32_e64 v10, 0, v213, s[26:27]
	v_cndmask_b32_e64 v10, v10, 1, s[28:29]
	v_add_u32_e32 v9, v9, v10
	s_and_b32 s27, vcc_hi, 0x10000000
	s_mov_b32 s26, s41
	s_cmp_eq_u64 s[26:27], 0
	s_cbranch_scc1 .LBB0_1049
